# P1: last in-proj GEMM unit prefetches the first K-tiles of the v_m GEMM unit; v_m GEMM skips its prologue loads
# baseline (speedup 1.0000x reference)
; template <class Epi, class Sched, bool ALIGN_EPI = false, bool SP2 = false, bool I8 = false>
; __device__ __forceinline__ void gemm_phase(PG8_LAS unsigned char* lds, const Gemm g, const Sched& S, const Epi& E) {
;     ...
;         const bool has_next = S.next(ui + 1, nxt);
;         const char* nA = has_next ? (const char*)g.A + (size_t)nxt.pm * tstep : cA; const char* nB = has_next ? (const char*)g.Bt + (size_t)nxt.pn * tstep : cB;
;         for (int t = 0; t < nt; t += 2) {
;             const bool last = (t == nt - 2);
;             const char* a1 = cA + (size_t)(t + 1) * kstep;
;             const char* a2 = last ? nA : cA + (size_t)(t + 2) * kstep; const char* b2 = last ? nB : cB + (size_t)(t + 2) * kstep;
; __global__ void __launch_bounds__(NWAVES * 64, 2) mk_fwd(Args args) {
;     ...
;         { pg8::Gemm g{(const pg8::bf16_t*)F.H1Q, F.WIN, M, NPROJ, D / 2}; pg8::StaticOrder S; S.init(M, NPROJ, F.G, (int)blockIdx.x);
;           pg8::EpiQ8 E{F.PROJ, NPROJ, 2048 / 256, F.SA, F.SW, 1};
;           pg8::gemm_phase<pg8::EpiQ8, pg8::StaticOrder, PG8_ALIGN, PG8_SP2, true>(F.lds, g, S, E); }
;         {
;           pg8::Gemm g{(const pg8::bf16_t*)((const unsigned char*)F.WIN + (size_t)WROW_VM * D), (const pg8::bf16_t*)F.H1Q, 1024, M, D / 2}; pg8::StaticOrder S; S.init(1024, M, F.G, (int)blockIdx.x);
;           pg8::EpiQ8 E{F.VT, M, 0, F.SW + WROW_VM, F.SA, 1};
;           pg8::gemm_phase<pg8::EpiQ8, pg8::StaticOrder, PG8_ALIGN, PG8_SP2, true>(F.lds, g, S, E); }
.LBB0_275:
	s_ashr_i32 s37, s36, 31
	s_lshl_b64 s[38:39], s[36:37], 19
	s_add_u32 s38, s60, s38
	s_addc_u32 s39, s61, s39
	s_and_b64 s[40:41], s[0:1], exec
	s_cselect_b32 s5, s39, s43
	s_cselect_b32 s33, s38, s42
	s_ashr_i32 s35, s34, 31
	s_lshl_b64 s[40:41], s[34:35], 19
	s_add_u32 s40, s10, s40
	s_addc_u32 s41, s11, s41
	s_and_b64 s[44:45], s[0:1], exec
	s_cselect_b32 s35, s41, s63
	s_cselect_b32 s37, s40, s62
	s_cbranch_scc1 .Lg1_keep
	v_readlane_b32 s40, v252, 11
	s_cmpk_lg_u32 s40, 0x100
	s_cbranch_scc1 .Lg1_keep
	s_and_b32 s40, s58, 7
	s_lshl_b32 s40, s40, 5
	s_lshr_b32 s41, s58, 3
	s_add_i32 s40, s40, s41
	s_and_b32 s41, s40, 3
	s_lshr_b32 s40, s40, 2
	s_lshl_b32 s41, s41, 19
	s_lshl_b32 s40, s40, 19
	s_add_u32 s33, s10, s41
	s_addc_u32 s5, s11, 0
	s_add_u32 s33, s33, 0xa00000
	s_addc_u32 s5, s5, 0
	s_add_u32 s37, s60, s40
	s_addc_u32 s35, s61, 0
.Lg1_keep:
	s_add_u32 s42, s42, 0x40080
	s_addc_u32 s43, s43, 0
	s_add_u32 s44, s62, 0x100
	v_mov_b32_e32 v2, 0
	s_addc_u32 s45, s63, 0
	s_mov_b32 s46, -2
	v_mov_b32_e32 v3, v2
	v_mov_b32_e32 v4, v2
	v_mov_b32_e32 v5, v2
	v_mov_b32_e32 v6, v2
	v_mov_b32_e32 v7, v2
	v_mov_b32_e32 v8, v2
	v_mov_b32_e32 v9, v2
	v_mov_b32_e32 v18, v2
	v_mov_b32_e32 v19, v2
	v_mov_b32_e32 v20, v2
	v_mov_b32_e32 v21, v2
	v_mov_b32_e32 v26, v2
	v_mov_b32_e32 v27, v2
	v_mov_b32_e32 v28, v2
	v_mov_b32_e32 v29, v2
	v_mov_b32_e32 v50, v2
	v_mov_b32_e32 v51, v2
	v_mov_b32_e32 v52, v2
	v_mov_b32_e32 v53, v2
	v_mov_b32_e32 v54, v2
	v_mov_b32_e32 v55, v2
	v_mov_b32_e32 v56, v2
	v_mov_b32_e32 v57, v2
	v_mov_b32_e32 v66, v2
	v_mov_b32_e32 v67, v2
	v_mov_b32_e32 v68, v2
	v_mov_b32_e32 v69, v2
	v_mov_b32_e32 v70, v2
	v_mov_b32_e32 v71, v2
	v_mov_b32_e32 v72, v2
	v_mov_b32_e32 v73, v2
	v_mov_b32_e32 v10, v2
	v_mov_b32_e32 v11, v2
	v_mov_b32_e32 v12, v2
	v_mov_b32_e32 v13, v2
	v_mov_b32_e32 v14, v2
	v_mov_b32_e32 v15, v2
	v_mov_b32_e32 v16, v2
	v_mov_b32_e32 v17, v2
	v_mov_b32_e32 v42, v2
	v_mov_b32_e32 v43, v2
	v_mov_b32_e32 v44, v2
	v_mov_b32_e32 v45, v2
	v_mov_b32_e32 v46, v2
	v_mov_b32_e32 v47, v2
	v_mov_b32_e32 v48, v2
	v_mov_b32_e32 v49, v2
	v_mov_b32_e32 v58, v2
	v_mov_b32_e32 v59, v2
	v_mov_b32_e32 v60, v2
	v_mov_b32_e32 v61, v2
	v_mov_b32_e32 v62, v2
	v_mov_b32_e32 v63, v2
	v_mov_b32_e32 v64, v2
	v_mov_b32_e32 v65, v2
	v_mov_b32_e32 v74, v2
	v_mov_b32_e32 v75, v2
	v_mov_b32_e32 v76, v2
	v_mov_b32_e32 v77, v2
	v_mov_b32_e32 v78, v2
	v_mov_b32_e32 v79, v2
	v_mov_b32_e32 v80, v2
	v_mov_b32_e32 v81, v2
	v_mov_b32_e32 v82, v2
	v_mov_b32_e32 v83, v2
	v_mov_b32_e32 v84, v2
	v_mov_b32_e32 v85, v2
	v_mov_b32_e32 v86, v2
	v_mov_b32_e32 v87, v2
	v_mov_b32_e32 v88, v2
	v_mov_b32_e32 v89, v2
	v_mov_b32_e32 v98, v2
	v_mov_b32_e32 v99, v2
	v_mov_b32_e32 v100, v2
	v_mov_b32_e32 v101, v2
	v_mov_b32_e32 v102, v2
	v_mov_b32_e32 v103, v2
	v_mov_b32_e32 v104, v2
	v_mov_b32_e32 v105, v2
	v_mov_b32_e32 v114, v2
	v_mov_b32_e32 v115, v2
	v_mov_b32_e32 v116, v2
	v_mov_b32_e32 v117, v2
	v_mov_b32_e32 v118, v2
	v_mov_b32_e32 v119, v2
	v_mov_b32_e32 v120, v2
	v_mov_b32_e32 v121, v2
	v_mov_b32_e32 v130, v2
	v_mov_b32_e32 v131, v2
	v_mov_b32_e32 v132, v2
	v_mov_b32_e32 v133, v2
	v_mov_b32_e32 v134, v2
	v_mov_b32_e32 v135, v2
	v_mov_b32_e32 v136, v2
	v_mov_b32_e32 v137, v2
	v_mov_b32_e32 v90, v2
	v_mov_b32_e32 v91, v2
	v_mov_b32_e32 v92, v2
	v_mov_b32_e32 v93, v2
	v_mov_b32_e32 v94, v2
	v_mov_b32_e32 v95, v2
	v_mov_b32_e32 v96, v2
	v_mov_b32_e32 v97, v2
	v_mov_b32_e32 v106, v2
	v_mov_b32_e32 v107, v2
	v_mov_b32_e32 v108, v2
	v_mov_b32_e32 v109, v2
	v_mov_b32_e32 v110, v2
	v_mov_b32_e32 v111, v2
	v_mov_b32_e32 v112, v2
	v_mov_b32_e32 v113, v2
	v_mov_b32_e32 v122, v2
	v_mov_b32_e32 v123, v2
	v_mov_b32_e32 v124, v2
	v_mov_b32_e32 v125, v2
	v_mov_b32_e32 v126, v2
	v_mov_b32_e32 v127, v2
	v_mov_b32_e32 v128, v2
	v_mov_b32_e32 v129, v2
	v_mov_b32_e32 v138, v2
	v_mov_b32_e32 v139, v2
	v_mov_b32_e32 v140, v2
	v_mov_b32_e32 v141, v2
	v_mov_b32_e32 v142, v2
	v_mov_b32_e32 v143, v2
	v_mov_b32_e32 v144, v2
	v_mov_b32_e32 v145, v2

; #define PG8_STAGE(bufoff, gbase, voff) do { _Pragma("unroll") for (int _i = 0; _i < 2; ++_i) \
;         __builtin_amdgcn_global_load_lds((const unsigned*)((const char*)(gbase) + (voff)[_i]), (PG8_LAS unsigned*)(lds + (bufoff) + ldsw + _i * 8192), 16, 0, 0); } while (0)
; #define PG8_WAIT_V(n) asm volatile("s_waitcnt vmcnt(" #n ")" ::: "memory")
; #define PG8_BAR __builtin_amdgcn_s_barrier()
; template <class Epi, class Sched, bool ALIGN_EPI = false, bool SP2 = false, bool I8 = false>
; __device__ __forceinline__ void gemm_phase(PG8_LAS unsigned char* lds, const Gemm g, const Sched& S, const Epi& E) {
;     ...
;     if constexpr (SP2) {
;         PG8_STAGE(PG8_SB(0, 0), cB, voffB); PG8_STAGE(PG8_SB(0, 1), cB + hstep, voffB); PG8_STAGE(PG8_SA(0, 0), cA, voffA); PG8_STAGE(PG8_SA(0, 1), cA + hstep, voffA);
;         if (wr == 1) PG8_BAR;
;         PG8_WAIT_V(2); PG8_BAR;
;         PG8_STAGE(PG8_SB(1, 0), cB + kstep, voffB); PG8_STAGE(PG8_SA(1, 0), cA + kstep, voffA); PG8_STAGE(PG8_SB(1, 1), cB + hstep + kstep, voffB);
;         PG8_WAIT_V(6); PG8_BAR;
; __global__ void __launch_bounds__(NWAVES * 64, 2) mk_fwd(Args args) {
;     ...
;           pg8::Gemm g{(const pg8::bf16_t*)((const unsigned char*)F.WIN + (size_t)WROW_VM * D), (const pg8::bf16_t*)F.H1Q, 1024, M, D / 2}; pg8::StaticOrder S; S.init(1024, M, F.G, (int)blockIdx.x);
;           pg8::EpiQ8 E{F.VT, M, 0, F.SW + WROW_VM, F.SA, 1};
;           pg8::gemm_phase<pg8::EpiQ8, pg8::StaticOrder, PG8_ALIGN, PG8_SP2, true>(F.lds, g, S, E); }
.LBB0_321:
	s_andn2_b64 vcc, exec, s[0:1]
	s_cbranch_vccnz .LBB0_373
	v_readlane_b32 s98, v252, 11
	v_readlane_b32 s0, v252, 13
	v_readlane_b32 s1, v252, 14
	s_add_u32 s17, s0, 0xe00000
	s_addc_u32 s19, s1, 0
	s_lshr_b32 s1, s14, 6
	s_ashr_i32 s5, s4, 31
	s_ashr_i32 s3, s2, 31
	s_lshr_b32 s0, s14, 8
	s_lshl_b32 s21, s1, 10
	s_lshl_b64 s[8:9], s[4:5], 19
	s_lshl_b64 s[10:11], s[2:3], 19
	s_add_u32 s42, s60, s10
	s_addc_u32 s43, s61, s11
	s_add_i32 s3, s21, 0
	s_add_i32 m0, s3, 0x10000
	v_mov_b32_e32 v155, 0
	s_cmpk_eq_u32 s98, 0x100
	s_cbranch_scc1 .Lg2_skip_13
	global_load_lds_dwordx4 v154, s[42:43]
.Lg2_skip_13:
	s_add_i32 m0, s3, 0x12000
	s_cmpk_eq_u32 s98, 0x100
	s_cbranch_scc1 .Lg2_skip_12
	global_load_lds_dwordx4 v158, s[42:43]
.Lg2_skip_12:
	s_add_u32 s10, s42, 0x40000
	s_addc_u32 s11, s43, 0
	s_add_i32 m0, s3, 0x14000
	v_mov_b32_e32 v159, v155
	s_cmpk_eq_u32 s98, 0x100
	s_cbranch_scc1 .Lg2_skip_11
	global_load_lds_dwordx4 v154, s[10:11]
.Lg2_skip_11:
	s_add_i32 m0, s3, 0x16000
	s_add_u32 s40, s17, s8
	s_addc_u32 s41, s19, s9
	s_add_i32 s23, s3, 0x2000
	s_cmpk_eq_u32 s98, 0x100
	s_cbranch_scc1 .Lg2_skip_10
	global_load_lds_dwordx4 v158, s[10:11]
.Lg2_skip_10:
	s_mov_b32 m0, s3
	s_cmpk_eq_u32 s98, 0x100
	s_cbranch_scc1 .Lg2_skip_9
	global_load_lds_dwordx4 v152, s[40:41]
.Lg2_skip_9:
	s_add_u32 s8, s40, 0x40000
	s_mov_b32 m0, s23
	s_addc_u32 s9, s41, 0
	s_add_i32 s25, s3, 0x4000
	s_cmpk_eq_u32 s98, 0x100
	s_cbranch_scc1 .Lg2_skip_8
	global_load_lds_dwordx4 v156, s[40:41]
.Lg2_skip_8:
	s_mov_b32 m0, s25
	s_add_i32 s27, s3, 0x6000
	s_cmpk_eq_u32 s98, 0x100
	s_cbranch_scc1 .Lg2_skip_7
	global_load_lds_dwordx4 v152, s[8:9]
.Lg2_skip_7:
	s_mov_b32 m0, s27
	v_mov_b32_e32 v153, v155
	s_cmpk_eq_u32 s98, 0x100
	s_cbranch_scc1 .Lg2_skip_6
	global_load_lds_dwordx4 v156, s[8:9]
.Lg2_skip_6:
	v_mov_b32_e32 v157, v155
	s_cmp_eq_u32 s0, 1
	s_mov_b32 s29, 0
	v_lshl_add_u64 v[8:9], s[42:43], 0, v[154:155]
	v_lshl_add_u64 v[6:7], s[42:43], 0, v[158:159]
	v_lshl_add_u64 v[2:3], s[40:41], 0, v[152:153]
	s_cselect_b64 s[8:9], -1, 0
	s_cmp_lg_u32 s0, 1
	v_lshl_add_u64 v[4:5], s[40:41], 0, v[156:157]
	s_cbranch_scc1 .LBB0_324
	s_barrier
.LBB0_324:
	v_readlane_b32 s10, v252, 13
	v_readlane_b32 s11, v252, 14
	s_add_u32 s10, s10, 0x3ec5000
	s_mov_b64 s[12:13], 0x80
	s_addc_u32 s11, s11, 0
	s_lshl_b32 s1, s1, 5
	s_add_i32 m0, s3, 0x18000
	v_lshl_add_u64 v[8:9], v[8:9], 0, s[12:13]
	s_lshl_b32 s5, s0, 13
	s_and_b32 s1, s1, 0x60
	s_waitcnt vmcnt(2)
	s_barrier
	s_cmpk_eq_u32 s98, 0x100
	s_cbranch_scc1 .Lg2_skip_5
	global_load_lds_dwordx4 v[8:9], off
.Lg2_skip_5:
	v_lshl_add_u64 v[6:7], v[6:7], 0, s[12:13]
	s_add_i32 m0, s3, 0x1a000
	s_add_i32 s68, s3, 0x8000
	s_add_i32 s69, s3, 0xa000
	s_cmpk_eq_u32 s98, 0x100
	s_cbranch_scc1 .Lg2_skip_4
	global_load_lds_dwordx4 v[6:7], off
.Lg2_skip_4:
	v_lshl_add_u64 v[2:3], v[2:3], 0, s[12:13]
	s_mov_b32 m0, s68
	s_cmpk_eq_u32 s98, 0x100
	s_cbranch_scc1 .Lg2_skip_3
	global_load_lds_dwordx4 v[2:3], off
.Lg2_skip_3:
	s_add_u32 s30, s42, 0x40080
	v_lshl_add_u64 v[2:3], v[4:5], 0, s[12:13]
	s_mov_b32 m0, s69
	s_addc_u32 s31, s43, 0
	s_cmpk_eq_u32 s98, 0x100
	s_cbranch_scc1 .Lg2_skip_2
	global_load_lds_dwordx4 v[2:3], off
.Lg2_skip_2:
	s_add_i32 m0, s3, 0x1c000
	v_lshl_add_u64 v[2:3], s[30:31], 0, v[154:155]
	s_cmpk_eq_u32 s98, 0x100
	s_cbranch_scc1 .Lg2_skip_1
	global_load_lds_dwordx4 v[2:3], off
.Lg2_skip_1:
	v_lshl_add_u64 v[2:3], s[30:31], 0, v[158:159]
	s_add_i32 m0, s3, 0x1e000
	v_lshlrev_b32_e32 v4, 11, v149
	s_cmpk_eq_u32 s98, 0x100
	s_cbranch_scc1 .Lg2_skip_0
	global_load_lds_dwordx4 v[2:3], off
.Lg2_skip_0:
	v_lshlrev_b32_e32 v3, 2, v197
	v_lshl_or_b32 v2, v197, 6, v198
	v_and_b32_e32 v3, 32, v3
	v_bitop3_b32 v2, v2, s5, v3 bitop3:0xde
	v_lshlrev_b32_e32 v3, 8, v0
	v_and_b32_e32 v3, 0x18000, v3
	v_or3_b32 v3, v1, v3, v4
	v_add_u32_e32 v160, v3, v147
	v_lshlrev_b32_e32 v3, 4, v151
	s_waitcnt vmcnt(6)
	s_cmpk_lt_u32 s14, 0x100
	v_and_b32_e32 v3, 0x38000, v3
	v_lshl_or_b32 v200, s0, 6, v197
	v_lshl_or_b32 v197, s1, 7, v199
	s_cselect_b64 s[14:15], -1, 0
	v_readlane_b32 s0, v252, 11
	v_or3_b32 v1, v1, v3, v4
	s_add_i32 s84, 0, 0x10000
	s_add_i32 s85, 0, 0x14000
	s_ashr_i32 s72, s0, 31
	s_ashr_i32 s73, s58, 31
	v_or_b32_e32 v196, s1, v196
	v_mov_b32_e32 v161, v155
	v_add_u32_e32 v162, v1, v147
	v_mov_b32_e32 v163, v155
	v_mov_b64_e32 v[164:165], 0x100
	v_mov_b64_e32 v[166:167], 0xff
	v_add_u32_e32 v1, s84, v197
	v_add_u32_e32 v147, s85, v197
	v_add_u32_e32 v149, 0, v2
	s_mov_b32 s16, 0x3e6d3388
	s_mov_b32 s18, 0x3f07dc22
	s_mov_b32 s20, 0xbf3a00e3
	s_mov_b32 s22, 0x3f35f0e3
	s_mov_b32 s24, 0xbe11a98e
	s_mov_b32 s26, 0x3e027906
	s_mov_b32 s28, 0xbf38aa3b
	s_barrier
	s_branch .LBB0_327

; __global__ void __launch_bounds__(NWAVES * 64, 2) mk_fwd(Args args) {
;     extern __shared__ __attribute__((aligned(16))) unsigned char lds[];
	.amdhsa_kernel _Z6mk_fwd4Args
		.amdhsa_group_segment_fixed_size 0
		.amdhsa_private_segment_fixed_size 0
		.amdhsa_kernarg_size 456
		.amdhsa_user_sgpr_count 2
		.amdhsa_user_sgpr_dispatch_ptr 0
		.amdhsa_user_sgpr_queue_ptr 0
		.amdhsa_user_sgpr_kernarg_segment_ptr 1
		.amdhsa_user_sgpr_dispatch_id 0
		.amdhsa_user_sgpr_kernarg_preload_length 0
		.amdhsa_user_sgpr_kernarg_preload_offset 0
		.amdhsa_user_sgpr_private_segment_size 0
		.amdhsa_uses_dynamic_stack 0
		.amdhsa_enable_private_segment 0
		.amdhsa_system_sgpr_workgroup_id_x 1
		.amdhsa_system_sgpr_workgroup_id_y 0
		.amdhsa_system_sgpr_workgroup_id_z 0
		.amdhsa_system_sgpr_workgroup_info 0
		.amdhsa_system_vgpr_workitem_id 0
		.amdhsa_next_free_vgpr 253
		.amdhsa_next_free_sgpr 100
		.amdhsa_accum_offset 256
		.amdhsa_reserve_vcc 1
		.amdhsa_float_round_mode_32 0
		.amdhsa_float_round_mode_16_64 0
		.amdhsa_float_denorm_mode_32 3
		.amdhsa_float_denorm_mode_16_64 3
		.amdhsa_dx10_clamp 1
		.amdhsa_ieee_mode 1
		.amdhsa_fp16_overflow 0
		.amdhsa_tg_split 0
		.amdhsa_exception_fp_ieee_invalid_op 0
		.amdhsa_exception_fp_denorm_src 0
		.amdhsa_exception_fp_ieee_div_zero 0
		.amdhsa_exception_fp_ieee_overflow 0
		.amdhsa_exception_fp_ieee_underflow 0
		.amdhsa_exception_fp_ieee_inexact 0
		.amdhsa_exception_int_div_zero 0
	.end_amdhsa_kernel

; __global__ void __launch_bounds__(NWAVES * 64, 2) mk_fwd(Args args) {
amdhsa.kernels:
  - .agpr_count:     0
    .args:
      - .offset:         0
        .size:           200
        .value_kind:     by_value
      - .offset:         200
        .size:           4
        .value_kind:     hidden_block_count_x
      - .offset:         204
        .size:           4
        .value_kind:     hidden_block_count_y
      - .offset:         208
        .size:           4
        .value_kind:     hidden_block_count_z
      - .offset:         212
        .size:           2
        .value_kind:     hidden_group_size_x
      - .offset:         214
        .size:           2
        .value_kind:     hidden_group_size_y
      - .offset:         216
        .size:           2
        .value_kind:     hidden_group_size_z
      - .offset:         218
        .size:           2
        .value_kind:     hidden_remainder_x
      - .offset:         220
        .size:           2
        .value_kind:     hidden_remainder_y
      - .offset:         222
        .size:           2
        .value_kind:     hidden_remainder_z
      - .offset:         240
        .size:           8
        .value_kind:     hidden_global_offset_x
      - .offset:         248
        .size:           8
        .value_kind:     hidden_global_offset_y
      - .offset:         256
        .size:           8
        .value_kind:     hidden_global_offset_z
      - .offset:         264
        .size:           2
        .value_kind:     hidden_grid_dims
      - .offset:         320
        .size:           4
        .value_kind:     hidden_dynamic_lds_size
    .group_segment_fixed_size: 0
    .kernarg_segment_align: 8
    .kernarg_segment_size: 456
    .language:       OpenCL C
    .language_version:
      - 2
      - 0
    .max_flat_workgroup_size: 512
    .name:           _Z6mk_fwd4Args
    .private_segment_fixed_size: 0
    .sgpr_count:     106
    .sgpr_spill_count: 73
    .symbol:         _Z6mk_fwd4Args.kd
    .uniform_work_group_size: 1
    .uses_dynamic_stack: false
    .vgpr_count:     253
    .vgpr_spill_count: 0
    .wavefront_size: 64
